# phase 0, 32-column weight items: the 8 masked dword gathers of a loop trip are issued together and waited once (was 32 serial load-wait-ds_write round trips per item) - stacked on v24
# baseline (speedup 1.0000x reference)
.LBB0_86:
	v_mov_b32_e32 v240, 0
	v_mov_b32_e32 v241, 0
	v_mov_b32_e32 v242, 0
	v_mov_b32_e32 v243, 0
	v_mov_b32_e32 v244, 0
	v_mov_b32_e32 v245, 0
	v_mov_b32_e32 v246, 0
	v_mov_b32_e32 v247, 0
	s_and_saveexec_b64 s[6:7], vcc
	s_cbranch_execz .Lp0s_issued
	v_lshl_add_u64 v[36:37], v[2:3], 2, s[0:1]
	global_load_dword v240, v[36:37], off
	v_lshl_add_u64 v[34:35], v[16:17], 0, s[4:5]
	global_load_dword v241, v[34:35], off
	v_lshl_add_u64 v[36:37], v[14:15], 0, s[4:5]
	global_load_dword v242, v[36:37], off
	v_lshl_add_u64 v[34:35], v[12:13], 0, s[4:5]
	global_load_dword v243, v[34:35], off
	v_lshl_add_u64 v[36:37], v[10:11], 0, s[4:5]
	global_load_dword v244, v[36:37], off
	v_lshl_add_u64 v[34:35], v[8:9], 0, s[4:5]
	global_load_dword v245, v[34:35], off
	v_lshl_add_u64 v[36:37], v[6:7], 0, s[4:5]
	global_load_dword v246, v[36:37], off
	v_lshl_add_u64 v[34:35], v[4:5], 0, s[4:5]
	global_load_dword v247, v[34:35], off
.Lp0s_issued:
	s_or_b64 exec, exec, s[6:7]
	s_waitcnt vmcnt(0)
	ds_write_b32 v33, v240
	ds_write_b32 v33, v241 offset:264
	ds_write_b32 v33, v242 offset:528
	ds_write_b32 v33, v243 offset:792
	ds_write_b32 v33, v244 offset:1056
	ds_write_b32 v33, v245 offset:1320
	ds_write_b32 v33, v246 offset:1584
	ds_write_b32 v33, v247 offset:1848
	s_add_u32 s4, s4, 0x16c600
	s_addc_u32 s5, s5, 0
	v_add_u32_e32 v33, 0x840, v33
	s_cmp_lg_u32 s4, 0x5b1800
	v_add_u32_e32 v2, 0x5b180, v2
	s_cbranch_scc0 .LBB0_64
	s_branch .LBB0_86
